# P3: next-unit prefetch issued after the unit's own loads and packed at unit end behind a counted wait (as in P5)
# speedup vs baseline: 1.0333x; 1.0059x over previous
.LBB0_337:
	s_or_b64 exec, exec, s[22:23]
	ds_write_b128 v32, v[16:19] offset:18432
	ds_write_b128 v32, v[12:15] offset:18448
	s_waitcnt lgkmcnt(0)
	s_barrier
	ds_read_b128 v[12:15], v22
	ds_read_b128 v[16:19], v31 offset:18432
	ds_read_b128 v[42:45], v22 offset:64
	ds_read_b128 v[46:49], v31 offset:18496
	ds_read_b128 v[50:53], v31 offset:20736
	ds_read_b128 v[54:57], v31 offset:20800
	ds_read_b128 v[58:61], v31 offset:23040
	ds_read_b128 v[62:65], v31 offset:23104
	v_lshlrev_b64 v[28:29], 22, v[28:29]
	ds_read_b128 v[66:69], v31 offset:25344
	ds_read_b128 v[70:73], v31 offset:25408
	ds_read_b128 v[74:77], v31 offset:27648
	ds_read_b128 v[78:81], v31 offset:27712
	ds_read_b128 v[82:85], v31 offset:29952
	ds_read_b128 v[86:89], v31 offset:30016
	ds_read_b128 v[90:93], v31 offset:32256
	ds_read_b128 v[94:97], v31 offset:32320
	ds_read_b128 v[98:101], v31 offset:34560
	ds_read_b128 v[102:105], v31 offset:34624
	v_lshl_add_u64 v[28:29], s[16:17], 0, v[28:29]
	s_lshl_b32 s14, s14, 15
	s_waitcnt lgkmcnt(14)
	v_mfma_f32_16x16x32_bf16 v[16:19], v[12:15], v[16:19], 0
	v_lshl_add_u64 v[28:29], v[28:29], 0, s[14:15]
	s_mov_b32 s19, s15
	v_lshl_add_u64 v[28:29], v[28:29], 0, s[18:19]
	s_waitcnt lgkmcnt(13)
	v_mfma_f32_16x16x32_bf16 v[50:53], v[12:15], v[50:53], 0
	v_mov_b32_e32 v25, v3
	v_lshl_add_u64 v[28:29], v[28:29], 0, v[24:25]
	v_mov_b32_e32 v27, v3
	s_waitcnt lgkmcnt(11)
	v_mfma_f32_16x16x32_bf16 v[58:61], v[12:15], v[58:61], 0
	v_lshl_add_u64 v[28:29], v[28:29], 0, v[26:27]
	s_add_i32 s83, s83, s24
	s_add_i32 s80, s80, s81
	s_waitcnt lgkmcnt(9)
	v_mfma_f32_16x16x32_bf16 v[66:69], v[12:15], v[66:69], 0
	s_waitcnt lgkmcnt(7)
	v_mfma_f32_16x16x32_bf16 v[74:77], v[12:15], v[74:77], 0
	s_waitcnt lgkmcnt(5)
	v_mfma_f32_16x16x32_bf16 v[82:85], v[12:15], v[82:85], 0
	s_waitcnt lgkmcnt(3)
	v_mfma_f32_16x16x32_bf16 v[90:93], v[12:15], v[90:93], 0
	s_waitcnt lgkmcnt(1)
	v_mfma_f32_16x16x32_bf16 v[12:15], v[12:15], v[98:101], 0
	v_mfma_f32_16x16x32_bf16 v[16:19], v[42:45], v[46:49], v[16:19]
	v_mfma_f32_16x16x32_bf16 v[46:49], v[42:45], v[54:57], v[50:53]
	v_mfma_f32_16x16x32_bf16 v[50:53], v[42:45], v[62:65], v[58:61]
	v_add_co_u32_e64 v62, s[0:1], s25, v28
	v_cvt_pk_bf16_f32 v58, v16, v17
	v_cvt_pk_bf16_f32 v59, v18, v19
	global_store_dwordx2 v[28:29], v[58:59], off
	s_nop 0
	v_addc_co_u32_e64 v63, s[0:1], 0, v29, s[0:1]
	v_cvt_pk_bf16_f32 v58, v46, v47
	v_cvt_pk_bf16_f32 v59, v48, v49
	s_movk_i32 s0, 0x4000
	v_mfma_f32_16x16x32_bf16 v[54:57], v[42:45], v[70:73], v[66:69]
	global_store_dwordx2 v[62:63], v[58:59], off offset:-4096
	v_cvt_pk_bf16_f32 v50, v50, v51
	v_cvt_pk_bf16_f32 v51, v52, v53
	v_mfma_f32_16x16x32_bf16 v[16:19], v[42:45], v[78:81], v[74:77]
	global_store_dwordx2 v[62:63], v[50:51], off
	v_cvt_pk_bf16_f32 v50, v54, v55
	v_cvt_pk_bf16_f32 v51, v56, v57
	v_mfma_f32_16x16x32_bf16 v[46:49], v[42:45], v[86:89], v[82:85]
	v_mfma_f32_16x16x32_bf16 v[58:61], v[42:45], v[94:97], v[90:93]
	s_waitcnt lgkmcnt(0)
	v_mfma_f32_16x16x32_bf16 v[12:15], v[42:45], v[102:105], v[12:15]
	v_add_co_u32_e64 v42, s[0:1], s0, v28
	s_nop 0
	v_addc_co_u32_e64 v43, s[0:1], 0, v29, s[0:1]
	global_store_dwordx2 v[42:43], v[50:51], off offset:-4096
	v_cvt_pk_bf16_f32 v16, v16, v17
	v_cvt_pk_bf16_f32 v17, v18, v19
	v_add_co_u32_e64 v18, s[0:1], s55, v28
	global_store_dwordx2 v[42:43], v[16:17], off
	v_cvt_pk_bf16_f32 v16, v46, v47
	v_cvt_pk_bf16_f32 v17, v48, v49
	s_nop 0
	v_addc_co_u32_e64 v19, s[0:1], 0, v29, s[0:1]
	global_store_dwordx2 v[18:19], v[16:17], off offset:-4096
	v_cvt_pk_bf16_f32 v16, v58, v59
	v_cvt_pk_bf16_f32 v17, v60, v61
	global_store_dwordx2 v[18:19], v[16:17], off
	v_cvt_pk_bf16_f32 v12, v12, v13
	v_cvt_pk_bf16_f32 v13, v14, v15
	v_add_co_u32_e64 v14, s[0:1], s82, v28
	s_nop 0
	v_addc_co_u32_e64 v15, s[0:1], 0, v29, s[0:1]
	s_add_i32 s0, s74, s83
	global_store_dwordx2 v[14:15], v[12:13], off
	s_cmpk_lt_i32 s0, 0x800
	s_waitcnt vmcnt(8)
	v_perm_b32 v33, v33, v128, s73
	v_perm_b32 v4, v4, v136, s73
	v_perm_b32 v34, v34, v129, s73
	v_perm_b32 v5, v5, v137, s73
	v_perm_b32 v35, v35, v130, s73
	v_perm_b32 v6, v6, v138, s73
	v_perm_b32 v36, v36, v131, s73
	v_perm_b32 v7, v7, v139, s73
	v_perm_b32 v37, v37, v132, s73
	v_perm_b32 v8, v8, v140, s73
	v_perm_b32 v38, v38, v133, s73
	v_perm_b32 v9, v9, v141, s73
	v_perm_b32 v39, v39, v134, s73
	v_perm_b32 v10, v10, v142, s73
	v_perm_b32 v40, v40, v135, s73
	v_perm_b32 v11, v11, v143, s73
	v_mov_b32_e32 v41, v36
	v_mov_b32_e32 v27, v39
	v_mov_b32_e32 v25, v40
	v_mov_b32_e32 v44, v33
	v_mov_b32_e32 v19, v7
	v_mov_b32_e32 v15, v11
	v_mov_b32_e32 v14, v10
	v_mov_b32_e32 v13, v9
	v_mov_b32_e32 v12, v8
	v_mov_b32_e32 v18, v6
	v_mov_b32_e32 v17, v5
	v_mov_b32_e32 v16, v4
	v_mov_b32_e32 v43, v34
	v_mov_b32_e32 v42, v35
	v_mov_b32_e32 v29, v37
	v_mov_b32_e32 v28, v38
	s_barrier
	s_cbranch_scc0 .LBB0_344
.LBB0_338:
.LBB0_340:
	s_add_i32 s14, s74, s83
	s_and_b32 s0, s14, 0x380
	v_or_b32_e32 v2, s0, v20
	v_lshlrev_b32_e32 v2, 2, v2
	v_lshl_add_u64 v[46:47], s[38:39], 0, v[2:3]
	s_movk_i32 s0, 0x1000
	v_add_co_u32_e64 v46, s[0:1], s0, v46
	v_lshlrev_b32_e32 v49, 16, v41
	s_nop 0
	v_addc_co_u32_e64 v47, s[0:1], 0, v47, s[0:1]
	global_load_dword v2, v2, s[38:39]
	s_nop 0
	global_load_dword v45, v[46:47], off
	v_lshlrev_b32_e32 v50, 16, v29
	v_lshlrev_b32_e32 v46, 16, v44
	v_mul_f32_e32 v49, 0xbfb8aa3b, v49
	v_mul_f32_e32 v50, 0xbfb8aa3b, v50
	v_and_b32_e32 v44, 0xffff0000, v44
	v_and_b32_e32 v29, 0xffff0000, v29
	v_mul_f32_e32 v46, 0xbfb8aa3b, v46
	v_exp_f32_e32 v49, v49
	v_exp_f32_e32 v50, v50
	v_lshlrev_b32_e32 v47, 16, v43
	v_lshlrev_b32_e32 v51, 16, v28
	v_and_b32_e32 v28, 0xffff0000, v28
	v_mul_f32_e32 v44, 0xbfb8aa3b, v44
	v_mul_f32_e32 v29, 0xbfb8aa3b, v29
	v_exp_f32_e32 v46, v46
	v_mul_f32_e32 v47, 0xbfb8aa3b, v47
	v_mul_f32_e32 v28, 0xbfb8aa3b, v28
	v_exp_f32_e32 v44, v44
	v_exp_f32_e32 v29, v29
	v_mul_f32_e32 v51, 0xbfb8aa3b, v51
	v_exp_f32_e32 v47, v47
	v_exp_f32_e32 v28, v28
	v_exp_f32_e32 v51, v51
	v_add_f32_e32 v49, 1.0, v49
	v_add_f32_e32 v50, 1.0, v50
	v_add_f32_e32 v46, 1.0, v46
	v_add_f32_e32 v44, 1.0, v44
	v_add_f32_e32 v29, 1.0, v29
	v_rcp_f32_e32 v46, v46
	v_add_f32_e32 v47, 1.0, v47
	v_add_f32_e32 v28, 1.0, v28
	v_rcp_f32_e32 v44, v44
	v_and_b32_e32 v43, 0xffff0000, v43
	v_add_f32_e32 v51, 1.0, v51
	v_rcp_f32_e32 v47, v47
	v_rcp_f32_e32 v28, v28
	v_lshlrev_b32_e32 v48, 16, v42
	v_and_b32_e32 v42, 0xffff0000, v42
	v_mul_f32_e32 v43, 0xbfb8aa3b, v43
	v_mul_f32_e32 v48, 0xbfb8aa3b, v48
	v_mul_f32_e32 v42, 0xbfb8aa3b, v42
	v_exp_f32_e32 v43, v43
	v_lshlrev_b32_e32 v52, 16, v27
	v_exp_f32_e32 v48, v48
	v_exp_f32_e32 v42, v42
	v_and_b32_e32 v41, 0xffff0000, v41
	v_mul_f32_e32 v52, 0xbfb8aa3b, v52
	v_mul_f32_e32 v41, 0xbfb8aa3b, v41
	v_exp_f32_e32 v52, v52
	v_exp_f32_e32 v41, v41
	v_add_f32_e32 v43, 1.0, v43
	v_add_f32_e32 v48, 1.0, v48
	v_add_f32_e32 v42, 1.0, v42
	v_rcp_f32_e32 v43, v43
	v_rcp_f32_e32 v48, v48
	v_rcp_f32_e32 v42, v42
	v_add_f32_e32 v41, 1.0, v41
	v_rcp_f32_e32 v41, v41
	v_and_b32_e32 v27, 0xffff0000, v27
	v_mul_f32_e32 v27, 0xbfb8aa3b, v27
	v_exp_f32_e32 v27, v27
	s_ashr_i32 s0, s14, 7
	v_add_f32_e32 v27, 1.0, v27
	v_rcp_f32_e32 v27, v27
	s_waitcnt vmcnt(0)
	s_add_i32 s98, s75, s83
	s_cmpk_gt_i32 s98, 0x7ff
	s_cbranch_scc1 .Lp3pf_done
	s_ashr_i32 s100, s98, 10
	s_ashr_i32 s101, s100, 31
	s_and_b32 s99, s80, 0x1fc0
	s_lshl_b64 s[100:101], s[100:101], 13
	v_or_b32_e32 v146, s99, v21
	v_or_b32_e32 v146, s100, v146
	v_mov_b64_e32 v[144:145], s[12:13]
	s_and_b32 s98, s98, 0x380
	s_lshl_b32 s98, s98, 1
	s_addk_i32 s98, 0x2000
	s_mov_b32 s99, 0
	v_mad_u64_u32 v[144:145], s[86:87], v146, s21, v[144:145]
	v_lshlrev_b32_e32 v148, 1, v20
	v_mov_b32_e32 v149, 0
	v_mad_i32_i24 v145, s101, v1, v145
	v_lshl_add_u64 v[148:149], v[148:149], 0, s[98:99]
	s_movk_i32 s100, 0x3800
	s_mov_b32 s101, 0
	v_lshl_add_u64 v[144:145], v[144:145], 0, v[148:149]
	global_load_ushort v128, v[144:145], off
	global_load_ushort v136, v[144:145], off offset:2048
	v_lshl_add_u64 v[144:145], v[144:145], 0, s[100:101]
	global_load_ushort v33, v[144:145], off
	global_load_ushort v4, v[144:145], off offset:2048
	v_lshl_add_u64 v[144:145], v[144:145], 0, s[100:101]
	global_load_ushort v129, v[144:145], off
	global_load_ushort v137, v[144:145], off offset:2048
	v_lshl_add_u64 v[144:145], v[144:145], 0, s[100:101]
	global_load_ushort v34, v[144:145], off
	global_load_ushort v5, v[144:145], off offset:2048
	v_lshl_add_u64 v[144:145], v[144:145], 0, s[100:101]
	global_load_ushort v130, v[144:145], off
	global_load_ushort v138, v[144:145], off offset:2048
	v_lshl_add_u64 v[144:145], v[144:145], 0, s[100:101]
	global_load_ushort v35, v[144:145], off
	global_load_ushort v6, v[144:145], off offset:2048
	v_lshl_add_u64 v[144:145], v[144:145], 0, s[100:101]
	global_load_ushort v131, v[144:145], off
	global_load_ushort v139, v[144:145], off offset:2048
	v_lshl_add_u64 v[144:145], v[144:145], 0, s[100:101]
	global_load_ushort v36, v[144:145], off
	global_load_ushort v7, v[144:145], off offset:2048
	v_lshl_add_u64 v[144:145], v[144:145], 0, s[100:101]
	global_load_ushort v132, v[144:145], off
	global_load_ushort v140, v[144:145], off offset:2048
	v_lshl_add_u64 v[144:145], v[144:145], 0, s[100:101]
	global_load_ushort v37, v[144:145], off
	global_load_ushort v8, v[144:145], off offset:2048
	v_lshl_add_u64 v[144:145], v[144:145], 0, s[100:101]
	global_load_ushort v133, v[144:145], off
	global_load_ushort v141, v[144:145], off offset:2048
	v_lshl_add_u64 v[144:145], v[144:145], 0, s[100:101]
	global_load_ushort v38, v[144:145], off
	global_load_ushort v9, v[144:145], off offset:2048
	v_lshl_add_u64 v[144:145], v[144:145], 0, s[100:101]
	global_load_ushort v134, v[144:145], off
	global_load_ushort v142, v[144:145], off offset:2048
	v_lshl_add_u64 v[144:145], v[144:145], 0, s[100:101]
	global_load_ushort v39, v[144:145], off
	global_load_ushort v10, v[144:145], off offset:2048
	v_lshl_add_u64 v[144:145], v[144:145], 0, s[100:101]
	global_load_ushort v135, v[144:145], off
	global_load_ushort v143, v[144:145], off offset:2048
	v_lshl_add_u64 v[144:145], v[144:145], 0, s[100:101]
	global_load_ushort v40, v[144:145], off
	global_load_ushort v11, v[144:145], off offset:2048
.Lp3pf_done:
	v_sub_f32_e32 v2, v45, v2
	v_mul_f32_e32 v2, 0x3fb8aa3b, v2
	v_exp_f32_e32 v2, v2
	v_rcp_f32_e32 v45, v49
	v_rcp_f32_e32 v49, v50
	v_add_f32_e32 v2, 1.0, v2
	v_rcp_f32_e32 v50, v2
	v_rcp_f32_e32 v2, v29
	v_rcp_f32_e32 v29, v51
	v_sub_f32_e32 v51, 1.0, v50
	v_fma_f32 v46, v46, v51, v50
	v_fma_f32 v44, v44, v51, v50
	v_fma_f32 v55, v2, v51, v50
	v_log_f32_e32 v2, v46
	v_fma_f32 v47, v47, v51, v50
	v_fma_f32 v57, v28, v51, v50
	v_log_f32_e32 v28, v44
	v_fma_f32 v56, v29, v51, v50
	v_log_f32_e32 v29, v47
	v_add_f32_e32 v2, 0, v2
	v_add_f32_e32 v64, v28, v2
	v_fma_f32 v53, v43, v51, v50
	v_add_f32_e32 v65, v29, v64
	v_add_f32_e32 v29, 1.0, v52
	v_rcp_f32_e32 v29, v29
	v_fma_f32 v48, v48, v51, v50
	v_fma_f32 v54, v42, v51, v50
	v_log_f32_e32 v42, v53
	v_log_f32_e32 v43, v48
	v_fma_f32 v45, v45, v51, v50
	v_log_f32_e32 v58, v54
	v_fma_f32 v68, v29, v51, v50
	v_lshlrev_b32_e32 v29, 16, v25
	v_fma_f32 v41, v41, v51, v50
	v_log_f32_e32 v59, v45
	v_mul_f32_e32 v29, 0xbfb8aa3b, v29
	v_and_b32_e32 v25, 0xffff0000, v25
	v_fma_f32 v49, v49, v51, v50
	v_log_f32_e32 v60, v41
	v_add_f32_e32 v66, v42, v65
	v_exp_f32_e32 v29, v29
	v_mul_f32_e32 v25, 0xbfb8aa3b, v25
	v_log_f32_e32 v61, v49
	v_add_f32_e32 v67, v43, v66
	v_exp_f32_e32 v25, v25
	v_log_f32_e32 v62, v55
	v_add_f32_e32 v58, v58, v67
	v_log_f32_e32 v63, v56
	v_add_f32_e32 v59, v59, v58
	v_add_f32_e32 v60, v60, v59
	v_log_f32_e32 v28, v57
	v_add_f32_e32 v29, 1.0, v29
	v_add_f32_e32 v61, v61, v60
	v_rcp_f32_e32 v29, v29
	v_add_f32_e32 v25, 1.0, v25
	v_add_f32_e32 v62, v62, v61
	v_rcp_f32_e32 v25, v25
	v_add_f32_e32 v63, v63, v62
	v_add_f32_e32 v52, v28, v63
	v_log_f32_e32 v28, v68
	v_fma_f32 v27, v27, v51, v50
	v_log_f32_e32 v42, v27
	v_fma_f32 v69, v29, v51, v50
	v_log_f32_e32 v29, v69
	v_fmac_f32_e32 v50, v25, v51
	v_log_f32_e32 v25, v50
	v_add_f32_e32 v51, v28, v52
	v_add_f32_e32 v70, v42, v51
	v_add_f32_e32 v71, v29, v70
	v_add_f32_e32 v25, v25, v71
	ds_write_b32 v191, v25 offset:36864
	s_waitcnt lgkmcnt(0)
	s_barrier
	ds_read2st64_b32 v[28:29], v30 offset0:144 offset1:146
	ds_read2st64_b32 v[42:43], v30 offset0:148 offset1:150
	v_sub_f32_e32 v41, 1.0, v41
	v_sub_f32_e32 v27, 1.0, v27
	s_waitcnt lgkmcnt(1)
	v_add_f32_e32 v28, 0, v28
	v_cndmask_b32_e64 v72, v28, 0, vcc
	v_add_f32_e32 v73, v29, v72
	v_cndmask_b32_e64 v72, v72, v73, s[6:7]
	s_waitcnt lgkmcnt(0)
	v_add_f32_e32 v73, v42, v72
	v_cndmask_b32_e64 v72, v72, v73, s[8:9]
	v_add_f32_e32 v73, v43, v72
	v_cndmask_b32_e64 v72, v72, v73, s[10:11]
	v_add_f32_e32 v73, v2, v72
	v_add_f32_e32 v2, v28, v29
	v_add_f32_e32 v2, v2, v42
	v_add_f32_e32 v2, v2, v43
	v_add_f32_e32 v64, v64, v72
	v_sub_f32_e32 v28, v2, v73
	v_exp_f32_e32 v28, v28
	v_sub_f32_e32 v29, v2, v64
	v_exp_f32_e32 v29, v29
	v_sub_f32_e32 v42, 1.0, v46
	v_mul_f32_e32 v28, v42, v28
	v_sub_f32_e32 v42, 1.0, v44
	v_add_f32_e32 v65, v65, v72
	v_mul_f32_e32 v29, v42, v29
	v_cvt_pk_bf16_f32 v28, v28, v29
	v_add_f32_e32 v66, v66, v72
	ds_write_b32 v32, v28
	v_sub_f32_e32 v28, v2, v65
	v_exp_f32_e32 v28, v28
	v_sub_f32_e32 v29, v2, v66
	v_exp_f32_e32 v29, v29
	v_sub_f32_e32 v42, 1.0, v47
	v_mul_f32_e32 v28, v42, v28
	v_sub_f32_e32 v42, 1.0, v53
	v_add_f32_e32 v67, v72, v67
	v_mul_f32_e32 v29, v42, v29
	v_cvt_pk_bf16_f32 v28, v28, v29
	v_add_f32_e32 v58, v72, v58
	ds_write_b32 v32, v28 offset:4
	v_sub_f32_e32 v28, v2, v67
	v_exp_f32_e32 v28, v28
	v_sub_f32_e32 v29, v2, v58
	v_exp_f32_e32 v29, v29
	v_sub_f32_e32 v42, 1.0, v48
	v_mul_f32_e32 v28, v42, v28
	v_sub_f32_e32 v42, 1.0, v54
	v_add_f32_e32 v59, v72, v59
	v_mul_f32_e32 v29, v42, v29
	v_cvt_pk_bf16_f32 v28, v28, v29
	v_add_f32_e32 v60, v72, v60
	ds_write_b32 v32, v28 offset:8
	v_sub_f32_e32 v28, v2, v59
	v_exp_f32_e32 v28, v28
	v_sub_f32_e32 v29, v2, v60
	v_exp_f32_e32 v29, v29
	v_sub_f32_e32 v42, 1.0, v45
	v_mul_f32_e32 v28, v42, v28
	v_add_f32_e32 v61, v72, v61
	v_mul_f32_e32 v29, v41, v29
	v_cvt_pk_bf16_f32 v28, v28, v29
	v_add_f32_e32 v62, v72, v62
	ds_write_b32 v32, v28 offset:12
	v_sub_f32_e32 v28, v2, v61
	v_exp_f32_e32 v28, v28
	v_sub_f32_e32 v29, v2, v62
	v_exp_f32_e32 v29, v29
	v_sub_f32_e32 v41, 1.0, v49
	v_mul_f32_e32 v28, v41, v28
	v_sub_f32_e32 v41, 1.0, v55
	v_add_f32_e32 v63, v72, v63
	v_mul_f32_e32 v29, v41, v29
	v_cvt_pk_bf16_f32 v28, v28, v29
	v_add_f32_e32 v52, v72, v52
	ds_write_b32 v32, v28 offset:16
	v_sub_f32_e32 v28, v2, v63
	v_exp_f32_e32 v28, v28
	v_sub_f32_e32 v29, v2, v52
	v_exp_f32_e32 v29, v29
	v_sub_f32_e32 v41, 1.0, v56
	v_mul_f32_e32 v28, v41, v28
	v_sub_f32_e32 v41, 1.0, v57
	v_add_f32_e32 v70, v72, v70
	v_mul_f32_e32 v29, v41, v29
	v_add_f32_e32 v51, v72, v51
	v_cvt_pk_bf16_f32 v28, v28, v29
	v_sub_f32_e32 v29, v2, v70
	ds_write_b32 v32, v28 offset:20
	v_sub_f32_e32 v28, v2, v51
	v_exp_f32_e32 v29, v29
	v_exp_f32_e32 v28, v28
	v_sub_f32_e32 v41, 1.0, v68
	v_add_f32_e32 v71, v72, v71
	v_mul_f32_e32 v27, v27, v29
	v_mul_f32_e32 v28, v41, v28
	v_cvt_pk_bf16_f32 v27, v28, v27
	v_add_f32_e32 v25, v72, v25
	ds_write_b32 v32, v27 offset:24
	v_sub_f32_e32 v27, v2, v71
	v_exp_f32_e32 v27, v27
	v_sub_f32_e32 v25, v2, v25
	v_exp_f32_e32 v25, v25
	v_sub_f32_e32 v28, 1.0, v69
	v_mul_f32_e32 v27, v28, v27
	v_sub_f32_e32 v28, 1.0, v50
	v_mul_f32_e32 v25, v28, v25
	v_cvt_pk_bf16_f32 v25, v27, v25
	ds_write_b32 v32, v25 offset:28
	s_and_saveexec_b64 s[22:23], s[4:5]
	s_xor_b64 s[22:23], exec, s[22:23]
	s_ashr_i32 s1, s0, 31
	s_or_saveexec_b64 s[22:23], s[22:23]
	s_and_b32 s14, s14, 0x7f
	v_mov_b64_e32 v[28:29], s[0:1]
	s_xor_b64 exec, exec, s[22:23]
	s_cbranch_execz .LBB0_337
	s_ashr_i32 s1, s0, 31
	s_lshl_b64 s[86:87], s[0:1], 16
	v_exp_f32_e32 v2, v2
	s_add_u32 s19, s71, s86
	s_addc_u32 s87, s72, s87
	s_lshl_b32 s86, s14, 9
	s_add_u32 s86, s19, s86
	s_addc_u32 s87, s87, 0
	v_mov_b64_e32 v[28:29], s[0:1]
	global_store_dword v23, v2, s[86:87]
	s_branch .LBB0_337
